# router token loop: counted wait leaves lane-0 result stores in flight across the back edge
# speedup vs baseline: 1.0119x; 1.0119x over previous
; __device__ __forceinline__ void router_ph(const int WID_, const bf16* __restrict__ x3, const float* __restrict__ nw, const float* __restrict__ wrg, const float* __restrict__ brg, ...
;     ...
;     for (int m = tile * 256 + wv; m < tile * 256 + 256; m += 8) {
;         float h[16]; float s = 0.f;
; #pragma unroll
;         for (int j = 0; j < 2; ++j) { const unsigned wd[4] = {nx[j].x, nx[j].y, nx[j].z, nx[j].w};
; #pragma unroll
;             for (int q = 0; q < 4; ++q) { const float lo = __builtin_bit_cast(float, wd[q] << 16), hi = __builtin_bit_cast(float, wd[q] & 0xffff0000u); h[8 * j + 2 * q] = lo; h[8 * j + 2 * q + 1] = hi; s += lo * lo + hi * hi; } }
;         { const int mn = min(m + 8, tile * 256 + 248 + wv); const uint4* xr = (const uint4*)(x3 + (size_t)mn * D);
; #pragma unroll
;           for (int j = 0; j < 2; ++j) nx[j] = xr[lane + 64 * j]; }
;         s = wave_sum(s);
;         const float rs = rsqrtf(s * (1.f / D) + 1e-6f);
;         float l1[4] = {0.f, 0.f, 0.f, 0.f};
; #pragma unroll
;         for (int j = 0; j < 2; ++j) {
;             const int k0 = (lane + 64 * j) * 8;
;             const float4 ga = gw[2 * j], gb = gw[2 * j + 1];
;             h[8 * j] *= rs * ga.x; h[8 * j + 1] *= rs * ga.y; h[8 * j + 2] *= rs * ga.z; h[8 * j + 3] *= rs * ga.w;
;             h[8 * j + 4] *= rs * gb.x; h[8 * j + 5] *= rs * gb.y; h[8 * j + 6] *= rs * gb.z; h[8 * j + 7] *= rs * gb.w;
; #pragma unroll
;             for (int e = 0; e < 8; ++e) { const h4 w = *(const h4*)(wg16 + (k0 + e) * 4); const float x = h[8 * j + e];
;                 l1[0] += x * (float)w[0]; l1[1] += x * (float)w[1]; l1[2] += x * (float)w[2]; l1[3] += x * (float)w[3]; }
;         }
; #pragma unroll
;         for (int i = 0; i < 4; ++i) l1[i] = wave_sum(l1[i]) + brg_l[i];
.LBB0_2145:
	v_and_b32_e32 v90, 0xffff0000, v16
	v_and_b32_e32 v92, 0xffff0000, v17
	v_lshlrev_b32_e32 v59, 16, v16
	v_mul_f32_e32 v14, v90, v90
	v_lshlrev_b32_e32 v91, 16, v17
	v_mul_f32_e32 v16, v92, v92
	v_fmac_f32_e32 v14, v59, v59
	v_fmac_f32_e32 v16, v91, v91
	v_and_b32_e32 v94, 0xffff0000, v18
	v_add_f32_e32 v14, v16, v14
	v_lshlrev_b32_e32 v93, 16, v18
	v_mul_f32_e32 v16, v94, v94
	v_fmac_f32_e32 v16, v93, v93
	v_and_b32_e32 v96, 0xffff0000, v19
	v_add_f32_e32 v14, v16, v14
	v_lshlrev_b32_e32 v95, 16, v19
	v_mul_f32_e32 v16, v96, v96
	v_and_b32_e32 v85, 0xffff0000, v13
	v_and_b32_e32 v84, 0xffff0000, v12
	v_fmac_f32_e32 v16, v95, v95
	v_lshlrev_b32_e32 v27, 16, v13
	v_lshlrev_b32_e32 v26, 16, v12
	v_pk_mul_f32 v[12:13], v[84:85], v[84:85]
	v_add_f32_e32 v14, v16, v14
	v_pk_fma_f32 v[16:17], v[26:27], v[26:27], v[12:13]
	v_and_b32_e32 v86, 0xffff0000, v2
	v_add_f32_e32 v14, v16, v14
	v_add_f32_e32 v88, v17, v14
	v_and_b32_e32 v14, 0xffff0000, v15
	v_lshlrev_b32_e32 v15, 16, v15
	v_lshlrev_b32_e32 v87, 16, v2
	v_mov_b32_e32 v82, v14
	v_mov_b32_e32 v83, v86
	v_mov_b32_e32 v80, v15
	v_mov_b32_e32 v81, v87
	v_pk_mul_f32 v[82:83], v[82:83], v[82:83]
	s_add_i32 s4, s44, 16
	v_pk_fma_f32 v[80:81], v[80:81], v[80:81], v[82:83]
	s_min_i32 s4, s4, s33
	v_add_f32_e32 v2, v81, v88
	v_add_f32_e32 v2, v80, v2
	v_mov_b32_e32 v80, 0
	s_ashr_i32 s5, s4, 31
	v_add_f32_dpp v2, v2, v2 quad_perm:[1,0,3,2] row_mask:0xf bank_mask:0xf bound_ctrl:1
	s_lshl_b64 s[4:5], s[4:5], 11
	v_lshl_add_u64 v[12:13], v[10:11], 0, s[4:5]
	v_add_f32_dpp v2, v2, v2 quad_perm:[2,3,0,1] row_mask:0xf bank_mask:0xf bound_ctrl:1
	ds_read_b128 v[16:19], v21 offset:256
	ds_read_b128 v[22:25], v52 offset:256
	ds_read_b128 v[60:63], v53 offset:256
	ds_read_b128 v[64:67], v54 offset:256
	ds_read_b128 v[68:71], v55 offset:256
	ds_read_b128 v[72:75], v56 offset:256
	ds_read_b128 v[76:79], v57 offset:256
	v_add_f32_dpp v2, v2, v2 row_half_mirror row_mask:0xf bank_mask:0xf bound_ctrl:1
	s_add_i32 s5, 0, 0x12100
	s_waitcnt lgkmcnt(0)
	v_cvt_f32_f16_sdwa v89, v77 dst_sel:DWORD dst_unused:UNUSED_PAD src0_sel:WORD_1
	v_add_f32_dpp v2, v2, v2 row_mirror row_mask:0xf bank_mask:0xf bound_ctrl:1
	v_cvt_f32_f16_sdwa v88, v79 dst_sel:DWORD dst_unused:UNUSED_PAD src0_sel:WORD_1
	s_nop 0
	v_mov_b32_dpp v80, v2 row_bcast:15 row_mask:0xa bank_mask:0xf
	v_add_f32_e32 v2, v2, v80
	v_mov_b32_e32 v80, 0
	s_nop 1
	v_mov_b32_dpp v80, v2 row_bcast:31 row_mask:0xc bank_mask:0xf
	v_add_f32_e32 v2, v2, v80
	s_nop 0
	v_readlane_b32 s4, v2, 63
	s_nop 1
	v_fma_f32 v2, s4, v196, v194
	v_mul_f32_e32 v80, 0x4b800000, v2
	v_cmp_gt_f32_e32 vcc, s64, v2
	s_nop 1
	v_cndmask_b32_e32 v2, v2, v80, vcc
	v_rsq_f32_e32 v2, v2
	ds_read_b128 v[80:83], v58 offset:256
	v_mul_f32_e32 v97, 0x45800000, v2
	v_cndmask_b32_e32 v2, v2, v97, vcc
	v_mul_f32_e32 v97, v29, v2
	v_mul_f32_e32 v97, v97, v59
	v_mul_f32_e32 v59, v31, v2
	v_mul_f32_e32 v90, v59, v90
	v_mul_f32_e32 v59, v30, v2
	v_mul_f32_e32 v91, v59, v91
	v_mul_f32_e32 v59, v3, v2
	v_mul_f32_e32 v92, v59, v92
	v_mul_f32_e32 v59, v33, v2
	v_mul_f32_e32 v93, v59, v93
	v_mul_f32_e32 v59, v32, v2
	v_mul_f32_e32 v94, v59, v94
	v_mul_f32_e32 v59, v6, v2
	v_mul_f32_e32 v95, v59, v95
	v_mul_f32_e32 v59, v7, v2
	v_mul_f32_e32 v96, v59, v96
	v_fma_mix_f32 v59, v97, v16, 0 op_sel_hi:[0,1,0]
	v_fma_mix_f32 v16, v97, v16, 0 op_sel:[0,1,0] op_sel_hi:[0,1,0]
	v_fma_mix_f32 v16, v90, v18, v16 op_sel:[0,1,0] op_sel_hi:[0,1,0]
	v_fma_mix_f32 v16, v91, v22, v16 op_sel:[0,1,0] op_sel_hi:[0,1,0]
	v_fma_mix_f32 v16, v92, v24, v16 op_sel:[0,1,0] op_sel_hi:[0,1,0]
	v_fma_mix_f32 v98, v97, v17, 0 op_sel_hi:[0,1,0]
	v_fma_mix_f32 v17, v97, v17, 0 op_sel:[0,1,0] op_sel_hi:[0,1,0]
	v_fma_mix_f32 v16, v93, v60, v16 op_sel:[0,1,0] op_sel_hi:[0,1,0]
	v_fma_mix_f32 v17, v90, v19, v17 op_sel:[0,1,0] op_sel_hi:[0,1,0]
	v_fma_mix_f32 v16, v94, v62, v16 op_sel:[0,1,0] op_sel_hi:[0,1,0]
	v_fma_mix_f32 v59, v90, v18, v59 op_sel_hi:[0,1,0]
	v_fma_mix_f32 v17, v91, v23, v17 op_sel:[0,1,0] op_sel_hi:[0,1,0]
	v_fma_mix_f32 v16, v95, v64, v16 op_sel:[0,1,0] op_sel_hi:[0,1,0]
	v_fma_mix_f32 v18, v90, v19, v98 op_sel_hi:[0,1,0]
	v_fma_mix_f32 v19, v91, v22, v59 op_sel_hi:[0,1,0]
	v_fma_mix_f32 v17, v92, v25, v17 op_sel:[0,1,0] op_sel_hi:[0,1,0]
	v_fma_mix_f32 v22, v96, v66, v16 op_sel:[0,1,0] op_sel_hi:[0,1,0]
	v_mul_f32_e32 v16, v8, v2
	v_fma_mix_f32 v18, v91, v23, v18 op_sel_hi:[0,1,0]
	v_fma_mix_f32 v19, v92, v24, v19 op_sel_hi:[0,1,0]
	v_fma_mix_f32 v17, v93, v61, v17 op_sel:[0,1,0] op_sel_hi:[0,1,0]
	v_mul_f32_e32 v98, v16, v26
	v_mul_f32_e32 v16, v9, v2
	v_fma_mix_f32 v18, v92, v25, v18 op_sel_hi:[0,1,0]
	v_fma_mix_f32 v19, v93, v60, v19 op_sel_hi:[0,1,0]
	v_fma_mix_f32 v17, v94, v63, v17 op_sel:[0,1,0] op_sel_hi:[0,1,0]
	v_mul_f32_e32 v84, v16, v84
	v_mul_f32_e32 v16, v35, v2
	v_fma_mix_f32 v18, v93, v61, v18 op_sel_hi:[0,1,0]
	v_fma_mix_f32 v19, v94, v62, v19 op_sel_hi:[0,1,0]
	v_fma_mix_f32 v17, v95, v65, v17 op_sel:[0,1,0] op_sel_hi:[0,1,0]
	v_mul_f32_e32 v99, v16, v27
	v_mul_f32_e32 v16, v34, v2
	v_fma_mix_f32 v18, v94, v63, v18 op_sel_hi:[0,1,0]
	v_fma_mix_f32 v19, v95, v64, v19 op_sel_hi:[0,1,0]
	v_fma_mix_f32 v23, v96, v67, v17 op_sel:[0,1,0] op_sel_hi:[0,1,0]
	v_mul_f32_e32 v85, v16, v85
	v_pk_mul_f32 v[16:17], v[0:1], v[2:3] op_sel_hi:[1,0]
	v_fma_mix_f32 v18, v95, v65, v18 op_sel_hi:[0,1,0]
	v_fma_mix_f32 v19, v96, v66, v19 op_sel_hi:[0,1,0]
	v_pk_mul_f32 v[26:27], v[16:17], v[86:87]
	v_pk_mul_f32 v[16:17], v[4:5], v[2:3] op_sel_hi:[1,0]
	v_fma_mix_f32 v18, v96, v67, v18 op_sel_hi:[0,1,0]
	v_pk_mul_f32 v[24:25], v[16:17], v[14:15]
	v_fma_mix_f32 v14, v98, v68, v19 op_sel_hi:[0,1,0]
	v_fma_mix_f32 v15, v98, v68, v22 op_sel:[0,1,0] op_sel_hi:[0,1,0]
	v_fma_mix_f32 v16, v98, v69, v18 op_sel_hi:[0,1,0]
	v_fma_mix_f32 v17, v98, v69, v23 op_sel:[0,1,0] op_sel_hi:[0,1,0]
	v_fma_mix_f32 v14, v84, v70, v14 op_sel_hi:[0,1,0]
	v_fma_mix_f32 v15, v84, v70, v15 op_sel:[0,1,0] op_sel_hi:[0,1,0]
	v_fma_mix_f32 v16, v84, v71, v16 op_sel_hi:[0,1,0]
	v_fma_mix_f32 v17, v84, v71, v17 op_sel:[0,1,0] op_sel_hi:[0,1,0]
	v_fma_mix_f32 v14, v99, v72, v14 op_sel_hi:[0,1,0]
	v_fma_mix_f32 v15, v99, v72, v15 op_sel:[0,1,0] op_sel_hi:[0,1,0]
	v_fma_mix_f32 v16, v99, v73, v16 op_sel_hi:[0,1,0]
	v_fma_mix_f32 v17, v99, v73, v17 op_sel:[0,1,0] op_sel_hi:[0,1,0]
	v_fma_mix_f32 v14, v85, v74, v14 op_sel_hi:[0,1,0]
	v_fma_mix_f32 v22, v85, v74, v15 op_sel:[0,1,0] op_sel_hi:[0,1,0]
	v_fma_mix_f32 v23, v85, v75, v16 op_sel_hi:[0,1,0]
	v_fma_mix_f32 v16, v85, v75, v17 op_sel:[0,1,0] op_sel_hi:[0,1,0]
	v_fma_mix_f32 v18, v27, v76, v14 op_sel_hi:[0,1,0]
	v_pk_mul_f32 v[14:15], v[26:27], v[88:89]
	v_cvt_f32_f16_sdwa v17, v76 dst_sel:DWORD dst_unused:UNUSED_PAD src0_sel:WORD_1
	v_add_f32_e32 v15, v15, v16
	v_cvt_f32_f16_sdwa v16, v78 dst_sel:DWORD dst_unused:UNUSED_PAD src0_sel:WORD_1
	v_fma_mix_f32 v59, v26, v78, v18 op_sel_hi:[0,1,0]
	v_cvt_f32_f16_e32 v19, v77
	v_cvt_f32_f16_e32 v18, v79
	v_pk_mul_f32 v[16:17], v[26:27], v[16:17]
	s_waitcnt lgkmcnt(0)
; __device__ __forceinline__ void router_ph(const int WID_, const bf16* __restrict__ x3, const float* __restrict__ nw, const float* __restrict__ wrg, const float* __restrict__ brg, ...
;     ...
;         int grp = 0; float best = l1[0];
; #pragma unroll
;         for (int i = 1; i < 4; ++i) if (l1[i] > best) { best = l1[i]; grp = i; }
;         float se = 0.f;
; #pragma unroll
;         for (int i = 0; i < 4; ++i) se += __expf(l1[i] - best);
;         const float g1 = 1.f / se;
;         float l2[8] = {};
;         const _Float16* we = we16 + (size_t)grp * D * 8;
; #pragma unroll
;         for (int j = 0; j < 2; ++j) {
;             const int k0 = (lane + 64 * j) * 8;
; #pragma unroll
;             for (int e = 0; e < 8; ++e) { const float x = h[8 * j + e]; const h8 w = *(const h8*)(we + (k0 + e) * 8);
; #pragma unroll
;                 for (int q = 0; q < 8; ++q) l2[q] += x * (float)w[q]; }
;         }
	v_fma_mix_f32 v59, v25, v80, v59 op_sel_hi:[0,1,0]
	v_add_f32_e32 v17, v17, v22
	v_add_f32_e32 v22, v16, v17
	v_pk_mul_f32 v[16:17], v[26:27], v[18:19]
	v_cvt_f32_f16_sdwa v19, v81 dst_sel:DWORD dst_unused:UNUSED_PAD src0_sel:WORD_1
	v_cvt_f32_f16_sdwa v18, v83 dst_sel:DWORD dst_unused:UNUSED_PAD src0_sel:WORD_1
	v_add_f32_e32 v17, v17, v23
	v_add_f32_e32 v23, v16, v17
	v_add_f32_e32 v16, v14, v15
	v_pk_mul_f32 v[14:15], v[24:25], v[18:19]
	v_cvt_f32_f16_sdwa v17, v80 dst_sel:DWORD dst_unused:UNUSED_PAD src0_sel:WORD_1
	v_add_f32_e32 v15, v15, v16
	v_cvt_f32_f16_sdwa v16, v82 dst_sel:DWORD dst_unused:UNUSED_PAD src0_sel:WORD_1
	v_cvt_f32_f16_e32 v19, v81
	v_cvt_f32_f16_e32 v18, v83
	v_fma_mix_f32 v59, v24, v82, v59 op_sel_hi:[0,1,0]
	v_pk_mul_f32 v[16:17], v[24:25], v[16:17]
	s_nop 0
	v_add_f32_e32 v17, v17, v22
	v_add_f32_e32 v22, v16, v17
	v_pk_mul_f32 v[16:17], v[24:25], v[18:19]
	v_add_f32_e32 v19, v14, v15
	v_add_f32_dpp v14, v59, v59 quad_perm:[1,0,3,2] row_mask:0xf bank_mask:0xf bound_ctrl:1
	v_mov_b32_e32 v15, 0
	v_add_f32_e32 v17, v17, v23
	v_add_f32_dpp v14, v14, v14 quad_perm:[2,3,0,1] row_mask:0xf bank_mask:0xf bound_ctrl:1
	v_add_f32_e32 v18, v16, v17
	v_mov_b32_e32 v23, 0
	v_add_f32_dpp v14, v14, v14 row_half_mirror row_mask:0xf bank_mask:0xf bound_ctrl:1
	s_nop 1
	v_add_f32_dpp v14, v14, v14 row_mirror row_mask:0xf bank_mask:0xf bound_ctrl:1
	s_nop 1
	v_mov_b32_dpp v15, v14 row_bcast:15 row_mask:0xa bank_mask:0xf
	v_add_f32_e32 v14, v14, v15
	v_mov_b32_e32 v15, 0
	s_nop 1
	v_mov_b32_dpp v15, v14 row_bcast:31 row_mask:0xc bank_mask:0xf
	v_add_f32_e32 v14, v14, v15
	v_mov_b32_e32 v15, 0
	v_readlane_b32 s4, v14, 63
	v_add_f32_dpp v14, v22, v22 quad_perm:[1,0,3,2] row_mask:0xf bank_mask:0xf bound_ctrl:1
	s_nop 1
	v_add_f32_dpp v14, v14, v14 quad_perm:[2,3,0,1] row_mask:0xf bank_mask:0xf bound_ctrl:1
	s_nop 1
	v_add_f32_dpp v14, v14, v14 row_half_mirror row_mask:0xf bank_mask:0xf bound_ctrl:1
	s_nop 1
	v_add_f32_dpp v14, v14, v14 row_mirror row_mask:0xf bank_mask:0xf bound_ctrl:1
	s_nop 1
	v_mov_b32_dpp v15, v14 row_bcast:15 row_mask:0xa bank_mask:0xf
	v_add_f32_e32 v22, v14, v15
	v_mov_b32_e32 v14, s5
	ds_read_b128 v[14:17], v14
	v_mov_b32_dpp v23, v22 row_bcast:31 row_mask:0xc bank_mask:0xf
	v_add_f32_e32 v22, v22, v23
	s_nop 0
	v_readlane_b32 s5, v22, 63
	s_waitcnt lgkmcnt(0)
	s_nop 0
	v_pk_add_f32 v[22:23], s[4:5], v[14:15]
	v_add_f32_dpp v14, v18, v18 quad_perm:[1,0,3,2] row_mask:0xf bank_mask:0xf bound_ctrl:1
	v_mov_b32_e32 v15, 0
	s_nop 0
	v_add_f32_dpp v14, v14, v14 quad_perm:[2,3,0,1] row_mask:0xf bank_mask:0xf bound_ctrl:1
	s_nop 1
	v_add_f32_dpp v14, v14, v14 row_half_mirror row_mask:0xf bank_mask:0xf bound_ctrl:1
	s_nop 1
	v_add_f32_dpp v14, v14, v14 row_mirror row_mask:0xf bank_mask:0xf bound_ctrl:1
	s_nop 1
	v_mov_b32_dpp v15, v14 row_bcast:15 row_mask:0xa bank_mask:0xf
	v_add_f32_e32 v14, v14, v15
	v_mov_b32_e32 v15, 0
	s_nop 1
	v_mov_b32_dpp v15, v14 row_bcast:31 row_mask:0xc bank_mask:0xf
	v_add_f32_e32 v14, v14, v15
	v_mov_b32_e32 v15, 0
	v_readlane_b32 s4, v14, 63
	v_add_f32_dpp v14, v19, v19 quad_perm:[1,0,3,2] row_mask:0xf bank_mask:0xf bound_ctrl:1
	s_nop 0
	v_add_f32_e32 v59, s4, v16
	v_add_f32_dpp v14, v14, v14 quad_perm:[2,3,0,1] row_mask:0xf bank_mask:0xf bound_ctrl:1
	s_nop 1
	v_add_f32_dpp v14, v14, v14 row_half_mirror row_mask:0xf bank_mask:0xf bound_ctrl:1
	s_nop 1
	v_add_f32_dpp v14, v14, v14 row_mirror row_mask:0xf bank_mask:0xf bound_ctrl:1
	s_nop 1
	v_mov_b32_dpp v15, v14 row_bcast:15 row_mask:0xa bank_mask:0xf
	v_add_f32_e32 v14, v14, v15
	v_mov_b32_e32 v15, 0
	s_nop 1
	v_mov_b32_dpp v15, v14 row_bcast:31 row_mask:0xc bank_mask:0xf
	v_add_f32_e32 v14, v14, v15
	s_nop 0
	v_readlane_b32 s4, v14, 63
	s_nop 1
	v_add_f32_e32 v60, s4, v17
	v_cmp_gt_f32_e64 s[4:5], v23, v22
	s_nop 1
	v_cndmask_b32_e64 v14, v22, v23, s[4:5]
	v_cmp_gt_f32_e64 s[6:7], v59, v14
	s_nop 1
	v_cndmask_b32_e64 v61, v14, v59, s[6:7]
	v_cndmask_b32_e64 v14, 0, 1, s[4:5]
	s_and_b64 s[4:5], s[6:7], exec
	v_cmp_gt_f32_e32 vcc, v60, v61
	v_readfirstlane_b32 s4, v14
	s_cselect_b32 s6, 2, s4
	s_and_b64 s[4:5], vcc, exec
	s_cselect_b32 s49, 3, s6
	s_lshl_b32 s4, s49, 14
	s_add_i32 s48, s4, 0
	global_load_dwordx4 v[16:19], v[12:13], off
	s_nop 0
	global_load_dwordx4 v[12:15], v[12:13], off offset:1024
	v_add_u32_e32 v112, s48, v36
	ds_read_b128 v[132:135], v112 offset:8448
	v_add_u32_e32 v113, s48, v37
	ds_read_b128 v[136:139], v113 offset:8448
	v_add_u32_e32 v112, s48, v38
	ds_read_b128 v[140:143], v112 offset:8448
	v_add_u32_e32 v113, s48, v39
	ds_read_b128 v[144:147], v113 offset:8448
	v_add_u32_e32 v112, s48, v40
	ds_read_b128 v[148:151], v112 offset:8448
	v_add_u32_e32 v113, s48, v41
	ds_read_b128 v[152:155], v113 offset:8448
	v_add_u32_e32 v112, s48, v42
	ds_read_b128 v[156:159], v112 offset:8448
	v_add_u32_e32 v113, s48, v43
	ds_read_b128 v[160:163], v113 offset:8448
	v_add_u32_e32 v112, s48, v44
	ds_read_b128 v[164:167], v112 offset:8448
	v_add_u32_e32 v113, s48, v45
	ds_read_b128 v[168:171], v113 offset:8448
	v_add_u32_e32 v112, s48, v46
	ds_read_b128 v[172:175], v112 offset:8448
	v_add_u32_e32 v113, s48, v47
	ds_read_b128 v[176:179], v113 offset:8448
	s_waitcnt lgkmcnt(11)
	v_fma_mix_f32 v70, v97, v132, 0 op_sel_hi:[0,1,0]
	v_fma_mix_f32 v71, v97, v132, 0 op_sel:[0,1,0] op_sel_hi:[0,1,0]
	v_fma_mix_f32 v72, v97, v133, 0 op_sel_hi:[0,1,0]
	v_fma_mix_f32 v73, v97, v133, 0 op_sel:[0,1,0] op_sel_hi:[0,1,0]
	v_fma_mix_f32 v74, v97, v134, 0 op_sel_hi:[0,1,0]
	v_fma_mix_f32 v75, v97, v134, 0 op_sel:[0,1,0] op_sel_hi:[0,1,0]
	v_fma_mix_f32 v76, v97, v135, 0 op_sel_hi:[0,1,0]
	v_fma_mix_f32 v77, v97, v135, 0 op_sel:[0,1,0] op_sel_hi:[0,1,0]
	s_waitcnt lgkmcnt(10)
; __device__ __forceinline__ void router_ph(const int WID_, const bf16* __restrict__ x3, const float* __restrict__ nw, const float* __restrict__ wrg, const float* __restrict__ brg, ...
;     ...
;         float l2[8] = {};
;         const _Float16* we = we16 + (size_t)grp * D * 8;
; #pragma unroll
;         for (int j = 0; j < 2; ++j) {
;             const int k0 = (lane + 64 * j) * 8;
; #pragma unroll
;             for (int e = 0; e < 8; ++e) { const float x = h[8 * j + e]; const h8 w = *(const h8*)(we + (k0 + e) * 8);
; #pragma unroll
;                 for (int q = 0; q < 8; ++q) l2[q] += x * (float)w[q]; }
;         }
	v_fma_mix_f32 v70, v90, v136, v70 op_sel_hi:[0,1,0]
	v_fma_mix_f32 v71, v90, v136, v71 op_sel:[0,1,0] op_sel_hi:[0,1,0]
	v_fma_mix_f32 v72, v90, v137, v72 op_sel_hi:[0,1,0]
	v_fma_mix_f32 v73, v90, v137, v73 op_sel:[0,1,0] op_sel_hi:[0,1,0]
	v_fma_mix_f32 v74, v90, v138, v74 op_sel_hi:[0,1,0]
	v_fma_mix_f32 v75, v90, v138, v75 op_sel:[0,1,0] op_sel_hi:[0,1,0]
	v_fma_mix_f32 v76, v90, v139, v76 op_sel_hi:[0,1,0]
	v_fma_mix_f32 v77, v90, v139, v77 op_sel:[0,1,0] op_sel_hi:[0,1,0]
	s_waitcnt lgkmcnt(9)
	v_fma_mix_f32 v70, v91, v140, v70 op_sel_hi:[0,1,0]
	v_fma_mix_f32 v71, v91, v140, v71 op_sel:[0,1,0] op_sel_hi:[0,1,0]
	v_fma_mix_f32 v72, v91, v141, v72 op_sel_hi:[0,1,0]
	v_fma_mix_f32 v73, v91, v141, v73 op_sel:[0,1,0] op_sel_hi:[0,1,0]
	v_fma_mix_f32 v74, v91, v142, v74 op_sel_hi:[0,1,0]
	v_fma_mix_f32 v75, v91, v142, v75 op_sel:[0,1,0] op_sel_hi:[0,1,0]
	v_fma_mix_f32 v76, v91, v143, v76 op_sel_hi:[0,1,0]
	v_fma_mix_f32 v77, v91, v143, v77 op_sel:[0,1,0] op_sel_hi:[0,1,0]
	s_waitcnt lgkmcnt(8)
	v_fma_mix_f32 v70, v92, v144, v70 op_sel_hi:[0,1,0]
	v_fma_mix_f32 v71, v92, v144, v71 op_sel:[0,1,0] op_sel_hi:[0,1,0]
	v_fma_mix_f32 v72, v92, v145, v72 op_sel_hi:[0,1,0]
	v_fma_mix_f32 v73, v92, v145, v73 op_sel:[0,1,0] op_sel_hi:[0,1,0]
	v_fma_mix_f32 v74, v92, v146, v74 op_sel_hi:[0,1,0]
	v_fma_mix_f32 v75, v92, v146, v75 op_sel:[0,1,0] op_sel_hi:[0,1,0]
	v_fma_mix_f32 v76, v92, v147, v76 op_sel_hi:[0,1,0]
	v_fma_mix_f32 v77, v92, v147, v77 op_sel:[0,1,0] op_sel_hi:[0,1,0]
	v_add_u32_e32 v112, s48, v48
	ds_read_b128 v[180:183], v112 offset:8448
	v_add_u32_e32 v113, s48, v49
	ds_read_b128 v[184:187], v113 offset:8448
	v_add_u32_e32 v112, s48, v50
	ds_read_b128 v[188:191], v112 offset:8448
	v_add_u32_e32 v113, s48, v51
	ds_read_b128 v[108:111], v113 offset:8448
	s_waitcnt lgkmcnt(11)
	v_fma_mix_f32 v70, v93, v148, v70 op_sel_hi:[0,1,0]
	v_fma_mix_f32 v71, v93, v148, v71 op_sel:[0,1,0] op_sel_hi:[0,1,0]
	v_fma_mix_f32 v72, v93, v149, v72 op_sel_hi:[0,1,0]
	v_fma_mix_f32 v73, v93, v149, v73 op_sel:[0,1,0] op_sel_hi:[0,1,0]
	v_fma_mix_f32 v74, v93, v150, v74 op_sel_hi:[0,1,0]
	v_fma_mix_f32 v75, v93, v150, v75 op_sel:[0,1,0] op_sel_hi:[0,1,0]
	v_fma_mix_f32 v76, v93, v151, v76 op_sel_hi:[0,1,0]
	v_fma_mix_f32 v77, v93, v151, v77 op_sel:[0,1,0] op_sel_hi:[0,1,0]
	s_waitcnt lgkmcnt(10)
	v_fma_mix_f32 v70, v94, v152, v70 op_sel_hi:[0,1,0]
	v_fma_mix_f32 v71, v94, v152, v71 op_sel:[0,1,0] op_sel_hi:[0,1,0]
	v_fma_mix_f32 v72, v94, v153, v72 op_sel_hi:[0,1,0]
	v_fma_mix_f32 v73, v94, v153, v73 op_sel:[0,1,0] op_sel_hi:[0,1,0]
	v_fma_mix_f32 v74, v94, v154, v74 op_sel_hi:[0,1,0]
	v_fma_mix_f32 v75, v94, v154, v75 op_sel:[0,1,0] op_sel_hi:[0,1,0]
	v_fma_mix_f32 v76, v94, v155, v76 op_sel_hi:[0,1,0]
	v_fma_mix_f32 v77, v94, v155, v77 op_sel:[0,1,0] op_sel_hi:[0,1,0]
	s_waitcnt lgkmcnt(9)
	v_fma_mix_f32 v70, v95, v156, v70 op_sel_hi:[0,1,0]
	v_fma_mix_f32 v71, v95, v156, v71 op_sel:[0,1,0] op_sel_hi:[0,1,0]
	v_fma_mix_f32 v72, v95, v157, v72 op_sel_hi:[0,1,0]
	v_fma_mix_f32 v73, v95, v157, v73 op_sel:[0,1,0] op_sel_hi:[0,1,0]
	v_fma_mix_f32 v74, v95, v158, v74 op_sel_hi:[0,1,0]
	v_fma_mix_f32 v75, v95, v158, v75 op_sel:[0,1,0] op_sel_hi:[0,1,0]
	v_fma_mix_f32 v76, v95, v159, v76 op_sel_hi:[0,1,0]
	v_fma_mix_f32 v77, v95, v159, v77 op_sel:[0,1,0] op_sel_hi:[0,1,0]
	s_waitcnt lgkmcnt(8)
	v_fma_mix_f32 v70, v96, v160, v70 op_sel_hi:[0,1,0]
	v_fma_mix_f32 v71, v96, v160, v71 op_sel:[0,1,0] op_sel_hi:[0,1,0]
	v_fma_mix_f32 v72, v96, v161, v72 op_sel_hi:[0,1,0]
	v_fma_mix_f32 v73, v96, v161, v73 op_sel:[0,1,0] op_sel_hi:[0,1,0]
	v_fma_mix_f32 v74, v96, v162, v74 op_sel_hi:[0,1,0]
	v_fma_mix_f32 v75, v96, v162, v75 op_sel:[0,1,0] op_sel_hi:[0,1,0]
	v_fma_mix_f32 v76, v96, v163, v76 op_sel_hi:[0,1,0]
	v_fma_mix_f32 v77, v96, v163, v77 op_sel:[0,1,0] op_sel_hi:[0,1,0]
	s_waitcnt lgkmcnt(7)
	v_fma_mix_f32 v70, v98, v164, v70 op_sel_hi:[0,1,0]
	v_fma_mix_f32 v71, v98, v164, v71 op_sel:[0,1,0] op_sel_hi:[0,1,0]
	v_fma_mix_f32 v72, v98, v165, v72 op_sel_hi:[0,1,0]
	v_fma_mix_f32 v73, v98, v165, v73 op_sel:[0,1,0] op_sel_hi:[0,1,0]
	v_fma_mix_f32 v74, v98, v166, v74 op_sel_hi:[0,1,0]
	v_fma_mix_f32 v75, v98, v166, v75 op_sel:[0,1,0] op_sel_hi:[0,1,0]
	v_fma_mix_f32 v76, v98, v167, v76 op_sel_hi:[0,1,0]
	v_fma_mix_f32 v77, v98, v167, v77 op_sel:[0,1,0] op_sel_hi:[0,1,0]
	s_waitcnt lgkmcnt(6)
	v_fma_mix_f32 v70, v84, v168, v70 op_sel_hi:[0,1,0]
	v_fma_mix_f32 v71, v84, v168, v71 op_sel:[0,1,0] op_sel_hi:[0,1,0]
	v_fma_mix_f32 v72, v84, v169, v72 op_sel_hi:[0,1,0]
	v_fma_mix_f32 v73, v84, v169, v73 op_sel:[0,1,0] op_sel_hi:[0,1,0]
	v_fma_mix_f32 v74, v84, v170, v74 op_sel_hi:[0,1,0]
	v_fma_mix_f32 v75, v84, v170, v75 op_sel:[0,1,0] op_sel_hi:[0,1,0]
	v_fma_mix_f32 v76, v84, v171, v76 op_sel_hi:[0,1,0]
	v_fma_mix_f32 v77, v84, v171, v77 op_sel:[0,1,0] op_sel_hi:[0,1,0]
	s_waitcnt lgkmcnt(5)
	v_fma_mix_f32 v70, v99, v172, v70 op_sel_hi:[0,1,0]
	v_fma_mix_f32 v71, v99, v172, v71 op_sel:[0,1,0] op_sel_hi:[0,1,0]
	v_fma_mix_f32 v72, v99, v173, v72 op_sel_hi:[0,1,0]
	v_fma_mix_f32 v73, v99, v173, v73 op_sel:[0,1,0] op_sel_hi:[0,1,0]
	v_fma_mix_f32 v74, v99, v174, v74 op_sel_hi:[0,1,0]
	v_fma_mix_f32 v75, v99, v174, v75 op_sel:[0,1,0] op_sel_hi:[0,1,0]
	v_fma_mix_f32 v76, v99, v175, v76 op_sel_hi:[0,1,0]
	v_fma_mix_f32 v77, v99, v175, v77 op_sel:[0,1,0] op_sel_hi:[0,1,0]
	s_waitcnt lgkmcnt(4)
	v_fma_mix_f32 v70, v85, v176, v70 op_sel_hi:[0,1,0]
	v_fma_mix_f32 v71, v85, v176, v71 op_sel:[0,1,0] op_sel_hi:[0,1,0]
	v_fma_mix_f32 v72, v85, v177, v72 op_sel_hi:[0,1,0]
	v_fma_mix_f32 v73, v85, v177, v73 op_sel:[0,1,0] op_sel_hi:[0,1,0]
	v_fma_mix_f32 v74, v85, v178, v74 op_sel_hi:[0,1,0]
	v_fma_mix_f32 v75, v85, v178, v75 op_sel:[0,1,0] op_sel_hi:[0,1,0]
	v_fma_mix_f32 v76, v85, v179, v76 op_sel_hi:[0,1,0]
	v_fma_mix_f32 v77, v85, v179, v77 op_sel:[0,1,0] op_sel_hi:[0,1,0]
	s_waitcnt lgkmcnt(3)
; template <int CTRL, int ROWMASK> __device__ __forceinline__ float dppf_(float x) { return __builtin_bit_cast(float, __builtin_amdgcn_update_dpp(0, __builtin_bit_cast(int, x), CTRL, ROWMASK, 0xf, false)); }
; __device__ __forceinline__ float wave_sum(float v) {
;     v += dppf_<0xB1, 0xf>(v); v += dppf_<0x4E, 0xf>(v); v += dppf_<0x141, 0xf>(v); v += dppf_<0x140, 0xf>(v);
;     v += dppf_<0x142, 0xa>(v);
;     v += dppf_<0x143, 0xc>(v);
;     return __builtin_bit_cast(float, __builtin_amdgcn_readlane(__builtin_bit_cast(int, v), 63));
; }
; __device__ __forceinline__ void router_ph(const int WID_, const bf16* __restrict__ x3, const float* __restrict__ nw, const float* __restrict__ wrg, const float* __restrict__ brg, ...
;     ...
;         for (int i = 0; i < 8; ++i) l2[i] = wave_sum(l2[i]) + bre_l[grp * 8 + i];
	v_fma_mix_f32 v70, v27, v180, v70 op_sel_hi:[0,1,0]
	v_fma_mix_f32 v71, v27, v180, v71 op_sel:[0,1,0] op_sel_hi:[0,1,0]
	v_fma_mix_f32 v72, v27, v181, v72 op_sel_hi:[0,1,0]
	v_fma_mix_f32 v73, v27, v181, v73 op_sel:[0,1,0] op_sel_hi:[0,1,0]
	v_fma_mix_f32 v74, v27, v182, v74 op_sel_hi:[0,1,0]
	v_fma_mix_f32 v75, v27, v182, v75 op_sel:[0,1,0] op_sel_hi:[0,1,0]
	v_fma_mix_f32 v76, v27, v183, v76 op_sel_hi:[0,1,0]
	v_fma_mix_f32 v77, v27, v183, v77 op_sel:[0,1,0] op_sel_hi:[0,1,0]
	s_waitcnt lgkmcnt(2)
	v_fma_mix_f32 v70, v26, v184, v70 op_sel_hi:[0,1,0]
	v_fma_mix_f32 v71, v26, v184, v71 op_sel:[0,1,0] op_sel_hi:[0,1,0]
	v_fma_mix_f32 v72, v26, v185, v72 op_sel_hi:[0,1,0]
	v_fma_mix_f32 v73, v26, v185, v73 op_sel:[0,1,0] op_sel_hi:[0,1,0]
	v_fma_mix_f32 v74, v26, v186, v74 op_sel_hi:[0,1,0]
	v_fma_mix_f32 v75, v26, v186, v75 op_sel:[0,1,0] op_sel_hi:[0,1,0]
	v_fma_mix_f32 v76, v26, v187, v76 op_sel_hi:[0,1,0]
	v_fma_mix_f32 v77, v26, v187, v77 op_sel:[0,1,0] op_sel_hi:[0,1,0]
	s_waitcnt lgkmcnt(1)
	v_fma_mix_f32 v70, v25, v188, v70 op_sel_hi:[0,1,0]
	v_fma_mix_f32 v71, v25, v188, v71 op_sel:[0,1,0] op_sel_hi:[0,1,0]
	v_fma_mix_f32 v72, v25, v189, v72 op_sel_hi:[0,1,0]
	v_fma_mix_f32 v73, v25, v189, v73 op_sel:[0,1,0] op_sel_hi:[0,1,0]
	v_fma_mix_f32 v74, v25, v190, v74 op_sel_hi:[0,1,0]
	v_fma_mix_f32 v75, v25, v190, v75 op_sel:[0,1,0] op_sel_hi:[0,1,0]
	v_fma_mix_f32 v76, v25, v191, v76 op_sel_hi:[0,1,0]
	v_fma_mix_f32 v77, v25, v191, v77 op_sel:[0,1,0] op_sel_hi:[0,1,0]
	s_waitcnt lgkmcnt(0)
	v_fma_mix_f32 v70, v24, v108, v70 op_sel_hi:[0,1,0]
	v_fma_mix_f32 v71, v24, v108, v71 op_sel:[0,1,0] op_sel_hi:[0,1,0]
	v_fma_mix_f32 v72, v24, v109, v72 op_sel_hi:[0,1,0]
	v_fma_mix_f32 v73, v24, v109, v73 op_sel:[0,1,0] op_sel_hi:[0,1,0]
	v_fma_mix_f32 v74, v24, v110, v74 op_sel_hi:[0,1,0]
	v_fma_mix_f32 v75, v24, v110, v75 op_sel:[0,1,0] op_sel_hi:[0,1,0]
	v_fma_mix_f32 v76, v24, v111, v76 op_sel_hi:[0,1,0]
	v_fma_mix_f32 v77, v24, v111, v77 op_sel:[0,1,0] op_sel_hi:[0,1,0]
	v_mov_b32_e32 v26, v70
	v_mov_b32_e32 v27, v71
	v_mov_b32_e32 v62, v72
	v_mov_b32_e32 v63, v73
	v_mov_b32_e32 v65, v74
	v_mov_b32_e32 v64, v75
	v_mov_b32_e32 v66, v76
	v_mov_b32_e32 v24, v77
	v_add_f32_dpp v26, v26, v26 quad_perm:[1,0,3,2] row_mask:0xf bank_mask:0xf bound_ctrl:1
	v_add_f32_dpp v27, v27, v27 quad_perm:[1,0,3,2] row_mask:0xf bank_mask:0xf bound_ctrl:1
	v_add_f32_dpp v62, v62, v62 quad_perm:[1,0,3,2] row_mask:0xf bank_mask:0xf bound_ctrl:1
	v_add_f32_dpp v63, v63, v63 quad_perm:[1,0,3,2] row_mask:0xf bank_mask:0xf bound_ctrl:1
	v_add_f32_dpp v65, v65, v65 quad_perm:[1,0,3,2] row_mask:0xf bank_mask:0xf bound_ctrl:1
	v_add_f32_dpp v64, v64, v64 quad_perm:[1,0,3,2] row_mask:0xf bank_mask:0xf bound_ctrl:1
	v_add_f32_dpp v66, v66, v66 quad_perm:[1,0,3,2] row_mask:0xf bank_mask:0xf bound_ctrl:1
	v_add_f32_dpp v24, v24, v24 quad_perm:[1,0,3,2] row_mask:0xf bank_mask:0xf bound_ctrl:1
	v_add_f32_dpp v26, v26, v26 quad_perm:[2,3,0,1] row_mask:0xf bank_mask:0xf bound_ctrl:1
	v_add_f32_dpp v27, v27, v27 quad_perm:[2,3,0,1] row_mask:0xf bank_mask:0xf bound_ctrl:1
	v_add_f32_dpp v62, v62, v62 quad_perm:[2,3,0,1] row_mask:0xf bank_mask:0xf bound_ctrl:1
	v_add_f32_dpp v63, v63, v63 quad_perm:[2,3,0,1] row_mask:0xf bank_mask:0xf bound_ctrl:1
	v_add_f32_dpp v65, v65, v65 quad_perm:[2,3,0,1] row_mask:0xf bank_mask:0xf bound_ctrl:1
	v_add_f32_dpp v64, v64, v64 quad_perm:[2,3,0,1] row_mask:0xf bank_mask:0xf bound_ctrl:1
	v_add_f32_dpp v66, v66, v66 quad_perm:[2,3,0,1] row_mask:0xf bank_mask:0xf bound_ctrl:1
	v_add_f32_dpp v24, v24, v24 quad_perm:[2,3,0,1] row_mask:0xf bank_mask:0xf bound_ctrl:1
	v_add_f32_dpp v26, v26, v26 row_half_mirror row_mask:0xf bank_mask:0xf bound_ctrl:1
	v_add_f32_dpp v27, v27, v27 row_half_mirror row_mask:0xf bank_mask:0xf bound_ctrl:1
	v_add_f32_dpp v62, v62, v62 row_half_mirror row_mask:0xf bank_mask:0xf bound_ctrl:1
	v_add_f32_dpp v63, v63, v63 row_half_mirror row_mask:0xf bank_mask:0xf bound_ctrl:1
	v_add_f32_dpp v65, v65, v65 row_half_mirror row_mask:0xf bank_mask:0xf bound_ctrl:1
	v_add_f32_dpp v64, v64, v64 row_half_mirror row_mask:0xf bank_mask:0xf bound_ctrl:1
	v_add_f32_dpp v66, v66, v66 row_half_mirror row_mask:0xf bank_mask:0xf bound_ctrl:1
	v_add_f32_dpp v24, v24, v24 row_half_mirror row_mask:0xf bank_mask:0xf bound_ctrl:1
	v_add_f32_dpp v26, v26, v26 row_mirror row_mask:0xf bank_mask:0xf bound_ctrl:1
	v_add_f32_dpp v27, v27, v27 row_mirror row_mask:0xf bank_mask:0xf bound_ctrl:1
	v_add_f32_dpp v62, v62, v62 row_mirror row_mask:0xf bank_mask:0xf bound_ctrl:1
	v_add_f32_dpp v63, v63, v63 row_mirror row_mask:0xf bank_mask:0xf bound_ctrl:1
	v_add_f32_dpp v65, v65, v65 row_mirror row_mask:0xf bank_mask:0xf bound_ctrl:1
	v_add_f32_dpp v64, v64, v64 row_mirror row_mask:0xf bank_mask:0xf bound_ctrl:1
	v_add_f32_dpp v66, v66, v66 row_mirror row_mask:0xf bank_mask:0xf bound_ctrl:1
	v_add_f32_dpp v24, v24, v24 row_mirror row_mask:0xf bank_mask:0xf bound_ctrl:1
	v_mov_b32_e32 v100, 0
	v_mov_b32_e32 v101, 0
	v_mov_b32_e32 v102, 0
	v_mov_b32_e32 v103, 0
	v_mov_b32_e32 v104, 0
	v_mov_b32_e32 v105, 0
	v_mov_b32_e32 v106, 0
	v_mov_b32_e32 v107, 0
	v_mov_b32_dpp v100, v26 row_bcast:15 row_mask:0xa bank_mask:0xf
	v_mov_b32_dpp v101, v27 row_bcast:15 row_mask:0xa bank_mask:0xf
	v_mov_b32_dpp v102, v62 row_bcast:15 row_mask:0xa bank_mask:0xf
	v_mov_b32_dpp v103, v63 row_bcast:15 row_mask:0xa bank_mask:0xf
	v_mov_b32_dpp v104, v65 row_bcast:15 row_mask:0xa bank_mask:0xf
	v_mov_b32_dpp v105, v64 row_bcast:15 row_mask:0xa bank_mask:0xf
	v_mov_b32_dpp v106, v66 row_bcast:15 row_mask:0xa bank_mask:0xf
	v_mov_b32_dpp v107, v24 row_bcast:15 row_mask:0xa bank_mask:0xf
; __device__ __forceinline__ void router_ph(const int WID_, const bf16* __restrict__ x3, const float* __restrict__ nw, const float* __restrict__ wrg, const float* __restrict__ brg, ...
;     ...
;         for (int i = 0; i < 8; ++i) l2[i] = wave_sum(l2[i]) + bre_l[grp * 8 + i];
;         int i0 = 0; float v0 = l2[0];
; #pragma unroll
;         for (int i = 1; i < 8; ++i) if (l2[i] > v0) { v0 = l2[i]; i0 = i; }
;         int i1 = -1; float v1 = -3.0e38f;
; #pragma unroll
;         for (int i = 0; i < 8; ++i) if (i != i0 && l2[i] > v1) { v1 = l2[i]; i1 = i; }
;         const float e1 = __expf(v1 - v0), inv = 1.f / (1.f + e1);
;         if (lane == 0) {
;             const int ea = grp * 8 + i0, eb = grp * 8 + i1;
;             mb.tok_e[2 * m] = ea; mb.tok_e[2 * m + 1] = eb; mb.tok_rs[m] = rs;
;             mb.tok_g[2 * m] = g1 * inv; mb.tok_g[2 * m + 1] = g1 * e1 * inv;
;             atomicAdd(&lcnt[ea], 1); atomicAdd(&lcnt[eb], 1);
;         }
	v_add_f32_e32 v26, v26, v100
	v_add_f32_e32 v27, v27, v101
	v_add_f32_e32 v62, v62, v102
	v_add_f32_e32 v63, v63, v103
	v_add_f32_e32 v65, v65, v104
	v_add_f32_e32 v64, v64, v105
	v_add_f32_e32 v66, v66, v106
	v_add_f32_e32 v24, v24, v107
	v_mov_b32_e32 v100, 0
	v_mov_b32_e32 v101, 0
	v_mov_b32_e32 v102, 0
	v_mov_b32_e32 v103, 0
	v_mov_b32_e32 v104, 0
	v_mov_b32_e32 v105, 0
	v_mov_b32_e32 v106, 0
	v_mov_b32_e32 v107, 0
	v_mov_b32_dpp v100, v26 row_bcast:31 row_mask:0xc bank_mask:0xf
	v_mov_b32_dpp v101, v27 row_bcast:31 row_mask:0xc bank_mask:0xf
	v_mov_b32_dpp v102, v62 row_bcast:31 row_mask:0xc bank_mask:0xf
	v_mov_b32_dpp v103, v63 row_bcast:31 row_mask:0xc bank_mask:0xf
	v_mov_b32_dpp v104, v65 row_bcast:31 row_mask:0xc bank_mask:0xf
	v_mov_b32_dpp v105, v64 row_bcast:31 row_mask:0xc bank_mask:0xf
	v_mov_b32_dpp v106, v66 row_bcast:31 row_mask:0xc bank_mask:0xf
	v_mov_b32_dpp v107, v24 row_bcast:31 row_mask:0xc bank_mask:0xf
	v_add_f32_e32 v26, v26, v100
	v_add_f32_e32 v27, v27, v101
	v_add_f32_e32 v62, v62, v102
	v_add_f32_e32 v63, v63, v103
	v_add_f32_e32 v65, v65, v104
	v_add_f32_e32 v64, v64, v105
	v_add_f32_e32 v66, v66, v106
	v_add_f32_e32 v24, v24, v107
	v_readlane_b32 s4, v26, 63
	v_readlane_b32 s5, v27, 63
	v_readlane_b32 s6, v62, 63
	v_readlane_b32 s7, v63, 63
	v_readlane_b32 s8, v65, 63
	v_readlane_b32 s9, v64, 63
	v_readlane_b32 s10, v66, 63
	v_readlane_b32 s11, v24, 63
	s_and_saveexec_b64 s[82:83], s[2:3]
	s_cbranch_execz .LBB0_2144
	s_mul_i32 s12, s49, 0xffffc020
	s_add_i32 s48, s48, s12
	v_mov_b32_e32 v62, s48
	ds_read_b128 v[24:27], v62 offset:128
	ds_read_b128 v[62:65], v62 offset:144
	s_waitcnt lgkmcnt(1)
	v_pk_add_f32 v[24:25], s[4:5], v[24:25]
	s_nop 0
	v_cmp_gt_f32_e64 s[4:5], v25, v24
	v_add_f32_e32 v26, s6, v26
	v_add_f32_e32 v27, s7, v27
	v_cndmask_b32_e64 v66, v24, v25, s[4:5]
	v_cmp_gt_f32_e64 s[6:7], v26, v66
	s_waitcnt lgkmcnt(0)
	v_add_f32_e32 v63, s9, v63
	v_add_f32_e32 v62, s8, v62
	v_cndmask_b32_e64 v66, v66, v26, s[6:7]
	v_cmp_gt_f32_e64 s[8:9], v27, v66
	v_add_f32_e32 v65, s11, v65
	v_add_f32_e32 v64, s10, v64
	v_cndmask_b32_e64 v66, v66, v27, s[8:9]
	v_cmp_gt_f32_e64 s[10:11], v62, v66
	v_cndmask_b32_e64 v67, 0, 1, s[4:5]
	s_nop 0
	v_cndmask_b32_e64 v66, v66, v62, s[10:11]
	v_cmp_gt_f32_e64 s[12:13], v63, v66
	s_nop 1
	v_cndmask_b32_e64 v66, v66, v63, s[12:13]
	v_cmp_gt_f32_e64 s[14:15], v64, v66
	s_nop 1
	v_cndmask_b32_e64 v66, v66, v64, s[14:15]
	v_cmp_ngt_f32_e64 s[16:17], v65, v66
	s_and_b64 s[22:23], s[14:15], s[16:17]
	s_and_b64 s[4:5], s[6:7], exec
	v_readfirstlane_b32 s4, v67
	s_cselect_b32 s6, 2, s4
	s_and_b64 s[4:5], s[8:9], exec
	s_cselect_b32 s6, 3, s6
	s_and_b64 s[4:5], s[10:11], exec
	s_cselect_b32 s6, 4, s6
	s_and_b64 s[4:5], s[12:13], exec
	s_cselect_b32 s6, 5, s6
	s_and_b64 s[4:5], s[14:15], exec
	s_cselect_b32 s6, 6, s6
	s_and_b64 s[4:5], s[16:17], exec
	s_cselect_b32 s46, s6, 7
	s_cmp_lg_u32 s46, 5
	s_cselect_b64 s[20:21], -1, 0
	s_cmp_lg_u32 s46, 4
	s_cselect_b64 s[14:15], -1, 0
	s_cmp_lg_u32 s46, 3
	s_cselect_b64 s[12:13], -1, 0
	s_cmp_lg_u32 s46, 2
	s_cselect_b64 s[10:11], -1, 0
	s_cmp_lg_u32 s46, 1
	s_cselect_b64 s[8:9], -1, 0
	s_cmp_eq_u32 s46, 0
	s_cselect_b64 s[6:7], -1, 0
	v_cmp_nlt_f32_e64 s[4:5], s34, v24
	s_or_b64 s[4:5], s[6:7], s[4:5]
	s_nop 0
	v_cndmask_b32_e64 v24, v24, v197, s[4:5]
	v_cmp_gt_f32_e64 s[6:7], v25, v24
	s_and_b64 s[6:7], s[8:9], s[6:7]
	s_nop 0
	v_cndmask_b32_e64 v24, v24, v25, s[6:7]
	v_cmp_gt_f32_e64 s[8:9], v26, v24
	s_and_b64 s[8:9], s[10:11], s[8:9]
	v_cndmask_b32_e64 v25, 0, -1, s[4:5]
	v_cndmask_b32_e64 v24, v24, v26, s[8:9]
	v_cndmask_b32_e32 v26, v61, v60, vcc
	v_sub_f32_e32 v22, v22, v26
	v_mul_f32_e32 v22, 0x3fb8aa3b, v22
	v_sub_f32_e32 v23, v23, v26
	v_exp_f32_e32 v22, v22
	v_mul_f32_e32 v23, 0x3fb8aa3b, v23
	v_exp_f32_e32 v23, v23
	v_cmp_gt_f32_e64 s[10:11], v27, v24
	s_and_b64 s[10:11], s[12:13], s[10:11]
	v_add_f32_e32 v22, 0, v22
	v_cndmask_b32_e64 v24, v24, v27, s[10:11]
	v_cmp_gt_f32_e64 s[12:13], v62, v24
	v_add_f32_e32 v22, v23, v22
	v_sub_f32_e32 v23, v59, v26
	s_and_b64 s[12:13], s[14:15], s[12:13]
	v_mul_f32_e32 v23, 0x3fb8aa3b, v23
	v_cndmask_b32_e64 v24, v24, v62, s[12:13]
	v_exp_f32_e32 v23, v23
	v_cmp_gt_f32_e64 s[14:15], v63, v24
	s_and_b64 s[14:15], s[20:21], s[14:15]
	v_add_f32_e32 v22, v23, v22
	v_cndmask_b32_e64 v24, v24, v63, s[14:15]
	v_cmp_ngt_f32_e64 s[20:21], v64, v24
	v_sub_f32_e32 v23, v60, v26
	s_or_b64 s[20:21], s[22:23], s[20:21]
	v_mul_f32_e32 v23, 0x3fb8aa3b, v23
	v_cndmask_b32_e64 v24, v64, v24, s[20:21]
	v_exp_f32_e32 v23, v23
	v_cmp_gt_f32_e64 s[22:23], v65, v24
	s_and_b64 s[22:23], s[16:17], s[22:23]
	s_and_b64 s[4:5], s[6:7], exec
	v_readfirstlane_b32 s4, v25
	v_add_f32_e32 v22, v23, v22
	s_cselect_b32 s6, 1, s4
	v_div_scale_f32 v23, s[4:5], v22, v22, 1.0
	v_rcp_f32_e32 v26, v23
	v_cndmask_b32_e64 v24, v24, v65, s[22:23]
	v_cndmask_b32_e64 v25, v65, v66, s[16:17]
	s_and_b64 s[4:5], s[8:9], exec
	v_fma_f32 v27, -v23, v26, 1.0
	v_fmac_f32_e32 v26, v27, v26
	v_div_scale_f32 v27, vcc, 1.0, v22, 1.0
	v_mul_f32_e32 v59, v27, v26
	v_fma_f32 v60, -v23, v59, v27
	v_fmac_f32_e32 v59, v60, v26
	v_fma_f32 v23, -v23, v59, v27
	v_div_fmas_f32 v23, v23, v26, v59
	v_div_fixup_f32 v26, v23, v22, 1.0
	v_sub_f32_e32 v22, v24, v25
	v_mul_f32_e32 v22, 0x3fb8aa3b, v22
	v_exp_f32_e32 v24, v22
	s_cselect_b32 s6, 2, s6
	s_and_b64 s[4:5], s[10:11], exec
	s_cselect_b32 s6, 3, s6
	v_add_f32_e32 v22, 1.0, v24
	v_div_scale_f32 v23, s[4:5], v22, v22, 1.0
	v_rcp_f32_e32 v25, v23
	s_and_b64 s[4:5], s[12:13], exec
	s_cselect_b32 s6, 4, s6
	s_and_b64 s[4:5], s[14:15], exec
	s_cselect_b32 s6, 5, s6
	s_and_b64 s[4:5], s[20:21], exec
	v_fma_f32 v27, -v23, v25, 1.0
	s_cselect_b32 s6, s6, 6
	s_and_b64 s[4:5], s[22:23], exec
	v_fmac_f32_e32 v25, v27, v25
	v_div_scale_f32 v27, vcc, 1.0, v22, 1.0
	s_cselect_b32 s8, 7, s6
	v_mul_f32_e32 v59, v27, v25
	s_lshl_b32 s4, s49, 3
	s_ashr_i32 s81, s80, 31
	v_fma_f32 v60, -v23, v59, v27
	s_or_b32 s9, s46, s4
	s_add_i32 s12, s8, s4
	s_lshl_b64 s[4:5], s[80:81], 2
	v_fmac_f32_e32 v59, v60, v25
	s_add_u32 s6, s52, s4
	v_fma_f32 v23, -v23, v59, v27
	s_addc_u32 s7, s53, s5
	s_add_i32 s10, s80, 1
	v_div_fmas_f32 v23, v23, v25, v59
	s_ashr_i32 s11, s10, 31
	v_div_fixup_f32 v25, v23, v22, 1.0
	v_mov_b32_e32 v22, s9
	v_mov_b32_e32 v23, s12
	s_add_u32 s4, s40, s4
	global_store_dwordx2 v129, v[22:23], s[6:7]
	global_store_dword v129, v2, s[78:79]
	v_mul_f32_e32 v2, v26, v25
	s_addc_u32 s5, s41, s5
	global_store_dword v129, v2, s[4:5]
	s_lshl_b64 s[4:5], s[10:11], 2
	v_mul_f32_e32 v2, v26, v24
	s_add_u32 s4, s40, s4
	v_mul_f32_e32 v2, v2, v25
	s_addc_u32 s5, s41, s5
	global_store_dword v129, v2, s[4:5]
	s_waitcnt vmcnt(4)
	s_mov_b64 s[4:5], exec
	v_mbcnt_lo_u32_b32 v2, s4, 0
	v_mbcnt_hi_u32_b32 v2, s5, v2
	v_cmp_eq_u32_e32 vcc, 0, v2
	s_and_saveexec_b64 s[6:7], vcc
	s_cbranch_execz .LBB0_2148
	s_lshl_b32 s9, s9, 2
	s_add_i32 s9, s9, 0
	s_bcnt1_i32_b64 s4, s[4:5]
	v_mov_b32_e32 v2, s9
	v_mov_b32_e32 v22, s4
	ds_add_u32 v2, v22

; __device__ __forceinline__ void router_ph(const int WID_, const bf16* __restrict__ x3, const float* __restrict__ nw, const float* __restrict__ wrg, const float* __restrict__ brg, ...
;     ...
;     for (int m = tile * 256 + wv; m < tile * 256 + 256; m += 8) {
.Lrt_b:
	s_or_b64 exec, exec, s[82:83]
	s_add_u32 s78, s78, 32
	s_addc_u32 s79, s79, 0
	s_add_i32 s80, s80, 16
	s_add_i32 s44, s44, 8
	s_cmp_ge_i32 s44, s43
	v_mov_b32_e32 v2, v14
	s_cbranch_scc0 .LBB0_2145
